# P12 tail: the 7 final-norm weight chunk loads issued together early instead of one per vmcnt(0) ladder step; the 8 output stores go out back to back
# speedup vs baseline: 1.0122x; 1.0066x over previous
.LBB0_1206:
	v_mov_b32_e32 v4, v127
	v_mov_b32_e32 v131, v126
	global_load_dwordx4 v[0:3], v5, s[14:15]
	global_load_dwordx4 v[6:9], v5, s[14:15] offset:16
	s_ashr_i32 s0, s42, 31
	s_lshr_b32 s0, s0, 20
	s_add_i32 s0, s42, s0
	s_lshr_b32 s0, s0, 12
	ds_read_b32 v10, v128
	s_mulk_i32 s0, 0x3000
	s_ashr_i32 s1, s0, 31
	s_lshl_b64 s[0:1], s[0:1], 2
	s_add_u32 s0, s2, s0
	s_addc_u32 s1, s3, s1
	s_waitcnt lgkmcnt(0)
	v_ashrrev_i32_e32 v11, 31, v10
	v_lshlrev_b64 v[10:11], 19, v[10:11]
	v_lshl_add_u64 v[10:11], s[10:11], 0, v[10:11]
	s_waitcnt vmcnt(0)
	v_readfirstlane_b32 s6, v0
	v_readfirstlane_b32 s7, v1
	v_readfirstlane_b32 s22, v2
	v_readfirstlane_b32 s26, v3
	v_readfirstlane_b32 s27, v6
	v_readfirstlane_b32 s29, v7
	v_readfirstlane_b32 s30, v8
	v_readfirstlane_b32 s31, v9
	s_bfe_u32 s33, s6, 0x100010
	s_lshl_b32 s6, s6, 11
	s_bfe_u32 s34, s7, 0x100010
	s_bfe_u32 s35, s22, 0x100010
	s_lshl_b32 s36, s22, 11
	s_bfe_u32 s37, s26, 0x100010
	s_bfe_u32 s38, s27, 0x100010
	s_bfe_u32 s39, s29, 0x100010
	s_bfe_u32 s40, s30, 0x100010
	s_bfe_u32 s41, s31, 0x100010
	s_lshl_b32 s33, s33, 2
	s_and_b32 s22, s6, 0x7fff800
	s_lshl_b32 s6, s34, 2
	s_lshl_b32 s34, s35, 2
	s_lshl_b32 s35, s37, 2
	s_lshl_b32 s37, s38, 2
	s_lshl_b32 s38, s39, 2
	s_lshl_b32 s39, s40, 2
	s_lshl_b32 s40, s41, 2
	s_add_i32 s33, s25, s33
	s_add_i32 s6, s25, s6
	s_add_i32 s34, s25, s34
	s_add_i32 s35, s25, s35
	s_add_i32 s37, s25, s37
	s_add_i32 s38, s25, s38
	s_add_i32 s39, s25, s39
	s_add_i32 s40, s25, s40
	v_mov_b32_e32 v0, s33
	v_mov_b32_e32 v1, s6
	v_readfirstlane_b32 s4, v10
	v_readfirstlane_b32 s5, v11
	v_mov_b32_e32 v3, s34
	v_mov_b32_e32 v7, s35
	v_mov_b32_e32 v9, s37
	v_mov_b32_e32 v11, s38
	v_mov_b32_e32 v13, s39
	v_mov_b32_e32 v15, s40
	ds_read_b32 v0, v0
	ds_read_b32 v2, v1
	ds_read_b32 v6, v3
	ds_read_b32 v8, v7
	ds_read_b32 v10, v9
	ds_read_b32 v12, v11
	ds_read_b32 v14, v13
	ds_read_b32 v18, v15
	s_waitcnt lgkmcnt(7)
	v_ashrrev_i32_e32 v1, 31, v0
	s_waitcnt lgkmcnt(6)
	v_ashrrev_i32_e32 v3, 31, v2
	v_lshlrev_b64 v[0:1], 19, v[0:1]
	s_lshl_b32 s7, s7, 11
	s_waitcnt lgkmcnt(5)
	v_ashrrev_i32_e32 v7, 31, v6
	v_lshlrev_b64 v[2:3], 19, v[2:3]
	v_lshl_add_u64 v[0:1], s[8:9], 0, v[0:1]
	s_waitcnt lgkmcnt(4)
	v_ashrrev_i32_e32 v9, 31, v8
	v_lshlrev_b64 v[6:7], 19, v[6:7]
	v_lshl_add_u64 v[2:3], s[8:9], 0, v[2:3]
	v_lshl_add_u64 v[136:137], v[0:1], 0, s[22:23]
	s_and_b32 s22, s7, 0x7fff800
	s_lshl_b32 s26, s26, 11
	s_waitcnt lgkmcnt(3)
	v_ashrrev_i32_e32 v11, 31, v10
	v_lshlrev_b64 v[8:9], 19, v[8:9]
	v_lshl_add_u64 v[6:7], s[8:9], 0, v[6:7]
	v_lshl_add_u64 v[140:141], v[2:3], 0, s[22:23]
	s_and_b32 s22, s36, 0x7fff800
	s_lshl_b32 s27, s27, 11
	s_waitcnt lgkmcnt(2)
	v_ashrrev_i32_e32 v13, 31, v12
	v_lshlrev_b64 v[10:11], 19, v[10:11]
	v_lshl_add_u64 v[8:9], s[8:9], 0, v[8:9]
	v_lshl_add_u64 v[148:149], v[6:7], 0, s[22:23]
	s_and_b32 s22, s26, 0x7fff800
	v_lshl_add_u64 v[10:11], s[8:9], 0, v[10:11]
	v_lshl_add_u64 v[64:65], v[8:9], 0, s[22:23]
	s_and_b32 s22, s27, 0x7fff800
	v_lshlrev_b64 v[6:7], 19, v[12:13]
	s_lshl_b32 s6, s29, 11
	v_lshl_add_u64 v[66:67], v[10:11], 0, s[22:23]
	s_and_b32 s22, s6, 0x7fff800
	v_lshl_add_u64 v[6:7], s[8:9], 0, v[6:7]
	s_waitcnt lgkmcnt(1)
	v_ashrrev_i32_e32 v15, 31, v14
	global_load_dwordx4 v[0:3], v131, s[4:5]
	v_lshl_add_u64 v[78:79], v[6:7], 0, s[22:23]
	v_lshlrev_b64 v[6:7], 19, v[14:15]
	global_load_dwordx4 v[14:17], v131, s[4:5] offset:1024
	s_lshl_b32 s4, s30, 11
	s_and_b32 s22, s4, 0x7fff800
	v_lshl_add_u64 v[6:7], s[8:9], 0, v[6:7]
	v_lshl_add_u64 v[6:7], v[6:7], 0, s[22:23]
	s_waitcnt lgkmcnt(0)
	v_ashrrev_i32_e32 v19, 31, v18
	v_readfirstlane_b32 s4, v6
	v_readfirstlane_b32 s5, v7
	v_lshlrev_b64 v[6:7], 19, v[18:19]
	v_lshl_add_u64 v[6:7], s[8:9], 0, v[6:7]
	s_waitcnt vmcnt(1)
	v_cvt_pk_f32_fp8_e32 v[110:111], v0
	s_nop 0
	global_load_dwordx4 v[10:13], v131, s[4:5]
	global_load_dwordx4 v[24:27], v131, s[4:5] offset:1024
	s_lshl_b32 s4, s31, 11
	s_and_b32 s22, s4, 0x7fff800
	v_lshl_add_u64 v[6:7], v[6:7], 0, s[22:23]
	s_add_u32 s0, s0, 0x10a000
	v_readfirstlane_b32 s4, v6
	v_readfirstlane_b32 s5, v7
	s_nop 4
	global_load_dwordx4 v[38:41], v131, s[4:5]
	global_load_dwordx4 v[50:53], v131, s[4:5] offset:1024
	v_readfirstlane_b32 s26, v64
	v_readfirstlane_b32 s27, v65
	s_nop 4
	global_load_dwordx4 v[244:247], v131, s[26:27]
	global_load_dwordx4 v[70:73], v131, s[26:27] offset:1024
	v_readfirstlane_b32 s26, v66
	v_readfirstlane_b32 s27, v67
	s_nop 4
	global_load_dwordx4 v[82:85], v131, s[26:27]
	global_load_dwordx4 v[86:89], v131, s[26:27] offset:1024
	v_readfirstlane_b32 s26, v78
	v_readfirstlane_b32 s27, v79
	s_nop 4
	global_load_dwordx4 v[102:105], v131, s[26:27]
	global_load_dwordx4 v[132:135], v131, s[26:27] offset:1024
	v_readfirstlane_b32 s26, v136
	v_readfirstlane_b32 s27, v137
	s_nop 4
	global_load_dwordx4 v[248:251], v131, s[26:27]
	global_load_dwordx4 v[136:139], v131, s[26:27] offset:1024
	v_readfirstlane_b32 s26, v140
	v_readfirstlane_b32 s27, v141
	s_nop 4
	global_load_dwordx4 v[140:143], v131, s[26:27]
	global_load_dwordx4 v[144:147], v131, s[26:27] offset:1024
	v_readfirstlane_b32 s26, v148
	v_readfirstlane_b32 s27, v149
	s_nop 4
	global_load_dwordx4 v[148:151], v131, s[26:27]
	global_load_dwordx4 v[252:255], v131, s[26:27] offset:1024
	s_load_dwordx4 s[4:7], s[96:97], 0xa8
	v_cvt_pk_f32_fp8_sdwa v[116:117], v0 src0_sel:WORD_1
	v_cvt_pk_f32_fp8_e32 v[112:113], v1
	v_cvt_pk_f32_fp8_sdwa v[118:119], v1 src0_sel:WORD_1
	v_cvt_pk_f32_fp8_e32 v[54:55], v2
	v_cvt_pk_f32_fp8_sdwa v[60:61], v2 src0_sel:WORD_1
	v_cvt_pk_f32_fp8_e32 v[42:43], v3
	v_cvt_pk_f32_fp8_sdwa v[44:45], v3 src0_sel:WORD_1
	s_waitcnt vmcnt(16)
	v_cvt_pk_f32_fp8_e32 v[30:31], v14
	v_cvt_pk_f32_fp8_sdwa v[32:33], v14 src0_sel:WORD_1
	v_cvt_pk_f32_fp8_e32 v[18:19], v15
	v_cvt_pk_f32_fp8_sdwa v[22:23], v15 src0_sel:WORD_1
	v_cvt_pk_f32_fp8_e32 v[2:3], v16
	v_cvt_pk_f32_fp8_sdwa v[8:9], v16 src0_sel:WORD_1
	v_cvt_pk_f32_fp8_e32 v[0:1], v17
	v_cvt_pk_f32_fp8_sdwa v[16:17], v17 src0_sel:WORD_1
	s_addc_u32 s1, s1, 0
	s_waitcnt vmcnt(15)
	v_cvt_pk_f32_fp8_e32 v[152:153], v10
	v_cvt_pk_f32_fp8_sdwa v[154:155], v10 src0_sel:WORD_1
	v_cvt_pk_f32_fp8_e32 v[156:157], v11
	v_cvt_pk_f32_fp8_sdwa v[158:159], v11 src0_sel:WORD_1
	v_cvt_pk_f32_fp8_e32 v[160:161], v12
	v_cvt_pk_f32_fp8_sdwa v[162:163], v12 src0_sel:WORD_1
	v_cvt_pk_f32_fp8_e32 v[62:63], v13
	v_cvt_pk_f32_fp8_sdwa v[68:69], v13 src0_sel:WORD_1
	s_waitcnt vmcnt(14)
	v_cvt_pk_f32_fp8_e32 v[46:47], v24
	v_cvt_pk_f32_fp8_sdwa v[48:49], v24 src0_sel:WORD_1
	v_cvt_pk_f32_fp8_e32 v[34:35], v25
	v_cvt_pk_f32_fp8_sdwa v[36:37], v25 src0_sel:WORD_1
	v_cvt_pk_f32_fp8_e32 v[20:21], v26
	v_cvt_pk_f32_fp8_sdwa v[24:25], v26 src0_sel:WORD_1
	v_cvt_pk_f32_fp8_e32 v[6:7], v27
	v_cvt_pk_f32_fp8_sdwa v[10:11], v27 src0_sel:WORD_1
	s_waitcnt vmcnt(13)
	v_cvt_pk_f32_fp8_e32 v[164:165], v38
	v_cvt_pk_f32_fp8_sdwa v[166:167], v38 src0_sel:WORD_1
	v_cvt_pk_f32_fp8_e32 v[168:169], v39
	v_cvt_pk_f32_fp8_sdwa v[170:171], v39 src0_sel:WORD_1
	v_cvt_pk_f32_fp8_e32 v[90:91], v40
	v_cvt_pk_f32_fp8_sdwa v[92:93], v40 src0_sel:WORD_1
	v_cvt_pk_f32_fp8_e32 v[74:75], v41
	v_cvt_pk_f32_fp8_sdwa v[76:77], v41 src0_sel:WORD_1
	s_waitcnt vmcnt(12)
	v_cvt_pk_f32_fp8_e32 v[56:57], v50
	v_cvt_pk_f32_fp8_sdwa v[58:59], v50 src0_sel:WORD_1
	v_cvt_pk_f32_fp8_e32 v[38:39], v51
	v_cvt_pk_f32_fp8_sdwa v[40:41], v51 src0_sel:WORD_1
	v_cvt_pk_f32_fp8_e32 v[26:27], v52
	v_cvt_pk_f32_fp8_sdwa v[28:29], v52 src0_sel:WORD_1
	v_cvt_pk_f32_fp8_e32 v[12:13], v53
	v_cvt_pk_f32_fp8_sdwa v[14:15], v53 src0_sel:WORD_1
	s_waitcnt vmcnt(11)
	v_cvt_pk_f32_fp8_e32 v[172:173], v244
	v_cvt_pk_f32_fp8_sdwa v[174:175], v244 src0_sel:WORD_1
	v_cvt_pk_f32_fp8_e32 v[176:177], v245
	v_cvt_pk_f32_fp8_sdwa v[178:179], v245 src0_sel:WORD_1
	v_cvt_pk_f32_fp8_e32 v[180:181], v246
	v_cvt_pk_f32_fp8_sdwa v[182:183], v246 src0_sel:WORD_1
	v_cvt_pk_f32_fp8_e32 v[106:107], v247
	v_cvt_pk_f32_fp8_sdwa v[108:109], v247 src0_sel:WORD_1
	s_waitcnt vmcnt(10)
	v_cvt_pk_f32_fp8_e32 v[94:95], v70
	v_cvt_pk_f32_fp8_sdwa v[96:97], v70 src0_sel:WORD_1
	v_cvt_pk_f32_fp8_e32 v[78:79], v71
	v_cvt_pk_f32_fp8_sdwa v[80:81], v71 src0_sel:WORD_1
	v_cvt_pk_f32_fp8_e32 v[64:65], v72
	v_cvt_pk_f32_fp8_sdwa v[66:67], v72 src0_sel:WORD_1
	v_cvt_pk_f32_fp8_e32 v[50:51], v73
	v_cvt_pk_f32_fp8_sdwa v[52:53], v73 src0_sel:WORD_1
	s_waitcnt vmcnt(9)
	v_cvt_pk_f32_fp8_e32 v[184:185], v82
	v_cvt_pk_f32_fp8_sdwa v[186:187], v82 src0_sel:WORD_1
	v_cvt_pk_f32_fp8_e32 v[188:189], v83
	v_cvt_pk_f32_fp8_sdwa v[190:191], v83 src0_sel:WORD_1
	v_cvt_pk_f32_fp8_e32 v[192:193], v84
	v_cvt_pk_f32_fp8_sdwa v[194:195], v84 src0_sel:WORD_1
	v_cvt_pk_f32_fp8_e32 v[196:197], v85
	v_cvt_pk_f32_fp8_sdwa v[198:199], v85 src0_sel:WORD_1
	s_waitcnt vmcnt(8)
	v_cvt_pk_f32_fp8_e32 v[114:115], v86
	v_cvt_pk_f32_fp8_sdwa v[120:121], v86 src0_sel:WORD_1
	v_cvt_pk_f32_fp8_e32 v[98:99], v87
	v_cvt_pk_f32_fp8_sdwa v[100:101], v87 src0_sel:WORD_1
	v_cvt_pk_f32_fp8_e32 v[82:83], v88
	v_cvt_pk_f32_fp8_sdwa v[84:85], v88 src0_sel:WORD_1
	v_cvt_pk_f32_fp8_e32 v[70:71], v89
	v_cvt_pk_f32_fp8_sdwa v[72:73], v89 src0_sel:WORD_1
	s_waitcnt vmcnt(7)
	v_cvt_pk_f32_fp8_e32 v[200:201], v102
	v_cvt_pk_f32_fp8_sdwa v[202:203], v102 src0_sel:WORD_1
	v_cvt_pk_f32_fp8_e32 v[204:205], v103
	v_cvt_pk_f32_fp8_sdwa v[206:207], v103 src0_sel:WORD_1
	v_cvt_pk_f32_fp8_e32 v[208:209], v104
	v_cvt_pk_f32_fp8_sdwa v[210:211], v104 src0_sel:WORD_1
	v_cvt_pk_f32_fp8_e32 v[212:213], v105
	v_cvt_pk_f32_fp8_sdwa v[214:215], v105 src0_sel:WORD_1
	s_waitcnt vmcnt(6)
	v_cvt_pk_f32_fp8_e32 v[216:217], v132
	v_cvt_pk_f32_fp8_sdwa v[218:219], v132 src0_sel:WORD_1
	v_cvt_pk_f32_fp8_e32 v[122:123], v133
	v_cvt_pk_f32_fp8_sdwa v[124:125], v133 src0_sel:WORD_1
	v_cvt_pk_f32_fp8_e32 v[102:103], v134
	v_cvt_pk_f32_fp8_sdwa v[104:105], v134 src0_sel:WORD_1
	v_cvt_pk_f32_fp8_e32 v[86:87], v135
	v_cvt_pk_f32_fp8_sdwa v[88:89], v135 src0_sel:WORD_1
	v_pk_add_f32 v[220:221], v[154:155], 0 op_sel_hi:[1,0]
	v_pk_add_f32 v[222:223], v[152:153], 0 op_sel_hi:[1,0]
	v_pk_add_f32 v[158:159], v[158:159], 0 op_sel_hi:[1,0]
	v_pk_add_f32 v[164:165], v[164:165], v[222:223]
	v_pk_add_f32 v[158:159], v[170:171], v[158:159]
	v_pk_add_f32 v[110:111], v[110:111], v[164:165]
	v_pk_add_f32 v[24:25], v[24:25], 0 op_sel_hi:[1,0]
	v_pk_add_f32 v[20:21], v[20:21], 0 op_sel_hi:[1,0]
	v_pk_add_f32 v[118:119], v[118:119], v[158:159]
	v_pk_add_f32 v[110:111], v[172:173], v[110:111]
	v_pk_add_f32 v[20:21], v[26:27], v[20:21]
	v_pk_add_f32 v[24:25], v[28:29], v[24:25]
	v_pk_add_f32 v[156:157], v[156:157], 0 op_sel_hi:[1,0]
	v_pk_add_f32 v[118:119], v[178:179], v[118:119]
	v_pk_add_f32 v[110:111], v[184:185], v[110:111]
	v_pk_add_f32 v[36:37], v[36:37], 0 op_sel_hi:[1,0]
	v_pk_add_f32 v[34:35], v[34:35], 0 op_sel_hi:[1,0]
	v_pk_add_f32 v[8:9], v[8:9], v[24:25]
	v_pk_add_f32 v[2:3], v[2:3], v[20:21]
	v_pk_add_f32 v[166:167], v[166:167], v[220:221]
	v_pk_add_f32 v[156:157], v[168:169], v[156:157]
	v_pk_add_f32 v[34:35], v[38:39], v[34:35]
	v_pk_add_f32 v[36:37], v[40:41], v[36:37]
	v_pk_add_f32 v[2:3], v[64:65], v[2:3]
	v_pk_add_f32 v[8:9], v[66:67], v[8:9]
	v_pk_add_f32 v[162:163], v[162:163], 0 op_sel_hi:[1,0]
	v_pk_add_f32 v[160:161], v[160:161], 0 op_sel_hi:[1,0]
	v_pk_add_f32 v[116:117], v[116:117], v[166:167]
	v_pk_add_f32 v[112:113], v[112:113], v[156:157]
	v_pk_add_f32 v[68:69], v[68:69], 0 op_sel_hi:[1,0]
	v_pk_add_f32 v[62:63], v[62:63], 0 op_sel_hi:[1,0]
	v_pk_add_f32 v[48:49], v[48:49], 0 op_sel_hi:[1,0]
	v_pk_add_f32 v[46:47], v[46:47], 0 op_sel_hi:[1,0]
	v_pk_add_f32 v[22:23], v[22:23], v[36:37]
	v_pk_add_f32 v[18:19], v[18:19], v[34:35]
	v_pk_add_f32 v[8:9], v[84:85], v[8:9]
	v_pk_add_f32 v[2:3], v[82:83], v[2:3]
	v_pk_add_f32 v[10:11], v[10:11], 0 op_sel_hi:[1,0]
	v_pk_add_f32 v[6:7], v[6:7], 0 op_sel_hi:[1,0]
	v_pk_add_f32 v[116:117], v[174:175], v[116:117]
	v_pk_add_f32 v[112:113], v[176:177], v[112:113]
	v_pk_add_f32 v[90:91], v[90:91], v[160:161]
	v_pk_add_f32 v[92:93], v[92:93], v[162:163]
	v_pk_add_f32 v[62:63], v[74:75], v[62:63]
	v_pk_add_f32 v[68:69], v[76:77], v[68:69]
	v_pk_add_f32 v[46:47], v[56:57], v[46:47]
	v_pk_add_f32 v[48:49], v[58:59], v[48:49]
	v_pk_add_f32 v[2:3], v[102:103], v[2:3]
	v_pk_add_f32 v[8:9], v[104:105], v[8:9]
	v_pk_add_f32 v[6:7], v[12:13], v[6:7]
	v_pk_add_f32 v[10:11], v[14:15], v[10:11]
	v_pk_add_f32 v[116:117], v[186:187], v[116:117]
	v_pk_add_f32 v[118:119], v[190:191], v[118:119]
	v_pk_add_f32 v[112:113], v[188:189], v[112:113]
	v_pk_add_f32 v[60:61], v[60:61], v[92:93]
	v_pk_add_f32 v[54:55], v[54:55], v[90:91]
	v_pk_add_f32 v[44:45], v[44:45], v[68:69]
	v_pk_add_f32 v[42:43], v[42:43], v[62:63]
	v_pk_add_f32 v[32:33], v[32:33], v[48:49]
	v_pk_add_f32 v[30:31], v[30:31], v[46:47]
	v_pk_add_f32 v[10:11], v[16:17], v[10:11]
	v_pk_add_f32 v[0:1], v[0:1], v[6:7]
	v_pk_add_f32 v[110:111], v[200:201], v[110:111]
	v_pk_add_f32 v[116:117], v[202:203], v[116:117]
	v_pk_add_f32 v[112:113], v[204:205], v[112:113]
	v_pk_add_f32 v[118:119], v[206:207], v[118:119]
	v_pk_add_f32 v[54:55], v[180:181], v[54:55]
	v_pk_add_f32 v[60:61], v[182:183], v[60:61]
	v_pk_add_f32 v[42:43], v[106:107], v[42:43]
	v_pk_add_f32 v[44:45], v[108:109], v[44:45]
	v_pk_add_f32 v[30:31], v[94:95], v[30:31]
	s_waitcnt vmcnt(5)
	v_cvt_pk_f32_fp8_e32 v[156:157], v248
	s_waitcnt vmcnt(4)
	v_cvt_pk_f32_fp8_e32 v[178:179], v138
	v_cvt_pk_f32_fp8_sdwa v[184:185], v138 src0_sel:WORD_1
	v_cvt_pk_f32_fp8_sdwa v[158:159], v248 src0_sel:WORD_1
	s_waitcnt vmcnt(2)
	v_cvt_pk_f32_fp8_e32 v[226:227], v146
	v_cvt_pk_f32_fp8_sdwa v[228:229], v146 src0_sel:WORD_1
	v_cvt_pk_f32_fp8_e32 v[164:165], v249
	v_cvt_pk_f32_fp8_sdwa v[132:133], v249 src0_sel:WORD_1
	v_cvt_pk_f32_fp8_e32 v[166:167], v250
	v_cvt_pk_f32_fp8_sdwa v[168:169], v250 src0_sel:WORD_1
	v_cvt_pk_f32_fp8_e32 v[170:171], v251
	v_cvt_pk_f32_fp8_sdwa v[134:135], v251 src0_sel:WORD_1
	v_cvt_pk_f32_fp8_e32 v[172:173], v136
	s_waitcnt vmcnt(0)
	v_cvt_pk_f32_fp8_e32 v[34:35], v254
	v_cvt_pk_f32_fp8_sdwa v[36:37], v254 src0_sel:WORD_1
	v_cvt_pk_f32_fp8_sdwa v[174:175], v136 src0_sel:WORD_1
	v_cvt_pk_f32_fp8_e32 v[176:177], v137
	v_cvt_pk_f32_fp8_sdwa v[136:137], v137 src0_sel:WORD_1
	v_cvt_pk_f32_fp8_e32 v[186:187], v139
	v_cvt_pk_f32_fp8_sdwa v[138:139], v139 src0_sel:WORD_1
	v_pk_add_f32 v[8:9], v[184:185], v[8:9]
	v_pk_add_f32 v[2:3], v[178:179], v[2:3]
	v_cvt_pk_f32_fp8_e32 v[188:189], v140
	v_cvt_pk_f32_fp8_sdwa v[190:191], v140 src0_sel:WORD_1
	v_cvt_pk_f32_fp8_e32 v[200:201], v141
	v_cvt_pk_f32_fp8_sdwa v[140:141], v141 src0_sel:WORD_1
	v_cvt_pk_f32_fp8_e32 v[202:203], v142
	v_cvt_pk_f32_fp8_sdwa v[204:205], v142 src0_sel:WORD_1
	v_cvt_pk_f32_fp8_e32 v[206:207], v143
	v_cvt_pk_f32_fp8_sdwa v[142:143], v143 src0_sel:WORD_1
	v_cvt_pk_f32_fp8_e32 v[220:221], v144
	v_cvt_pk_f32_fp8_sdwa v[222:223], v144 src0_sel:WORD_1
	v_cvt_pk_f32_fp8_e32 v[224:225], v145
	v_cvt_pk_f32_fp8_sdwa v[144:145], v145 src0_sel:WORD_1
	v_cvt_pk_f32_fp8_e32 v[230:231], v147
	v_cvt_pk_f32_fp8_sdwa v[146:147], v147 src0_sel:WORD_1
	v_pk_add_f32 v[32:33], v[96:97], v[32:33]
	v_pk_add_f32 v[18:19], v[78:79], v[18:19]
	v_pk_add_f32 v[22:23], v[80:81], v[22:23]
	v_pk_add_f32 v[2:3], v[226:227], v[2:3]
	v_pk_add_f32 v[8:9], v[228:229], v[8:9]
	v_pk_add_f32 v[0:1], v[50:51], v[0:1]
	v_pk_add_f32 v[6:7], v[52:53], v[10:11]
	v_cvt_pk_f32_fp8_e32 v[232:233], v148
	v_cvt_pk_f32_fp8_sdwa v[234:235], v148 src0_sel:WORD_1
	v_cvt_pk_f32_fp8_e32 v[236:237], v149
	v_cvt_pk_f32_fp8_sdwa v[148:149], v149 src0_sel:WORD_1
	v_cvt_pk_f32_fp8_e32 v[238:239], v150
	v_cvt_pk_f32_fp8_sdwa v[240:241], v150 src0_sel:WORD_1
	v_pk_add_f32 v[60:61], v[194:195], v[60:61]
	v_pk_add_f32 v[54:55], v[192:193], v[54:55]
	v_cvt_pk_f32_fp8_e32 v[90:91], v151
	v_cvt_pk_f32_fp8_sdwa v[92:93], v151 src0_sel:WORD_1
	v_pk_add_f32 v[44:45], v[198:199], v[44:45]
	v_pk_add_f32 v[42:43], v[196:197], v[42:43]
	v_cvt_pk_f32_fp8_e32 v[62:63], v252
	v_cvt_pk_f32_fp8_sdwa v[68:69], v252 src0_sel:WORD_1
	v_pk_add_f32 v[32:33], v[120:121], v[32:33]
	v_pk_add_f32 v[30:31], v[114:115], v[30:31]
	v_cvt_pk_f32_fp8_e32 v[46:47], v253
	v_cvt_pk_f32_fp8_sdwa v[48:49], v253 src0_sel:WORD_1
	v_pk_add_f32 v[22:23], v[100:101], v[22:23]
	v_pk_add_f32 v[18:19], v[98:99], v[18:19]
	v_pk_add_f32 v[20:21], v[36:37], v[8:9]
	v_pk_add_f32 v[24:25], v[34:35], v[2:3]
	v_cvt_pk_f32_fp8_e32 v[2:3], v255
	v_cvt_pk_f32_fp8_sdwa v[8:9], v255 src0_sel:WORD_1
	v_pk_add_f32 v[6:7], v[72:73], v[6:7]
	v_pk_add_f32 v[0:1], v[70:71], v[0:1]
	v_pk_add_f32 v[54:55], v[208:209], v[54:55]
	v_pk_add_f32 v[60:61], v[210:211], v[60:61]
	v_pk_add_f32 v[42:43], v[212:213], v[42:43]
	v_pk_add_f32 v[44:45], v[214:215], v[44:45]
	v_pk_add_f32 v[30:31], v[216:217], v[30:31]
	v_pk_add_f32 v[32:33], v[218:219], v[32:33]
	v_pk_add_f32 v[18:19], v[122:123], v[18:19]
	v_pk_add_f32 v[22:23], v[124:125], v[22:23]
	v_pk_add_f32 v[0:1], v[86:87], v[0:1]
	v_pk_add_f32 v[6:7], v[88:89], v[6:7]
	v_pk_add_f32 v[116:117], v[158:159], v[116:117]
	v_pk_add_f32 v[110:111], v[156:157], v[110:111]
	v_pk_add_f32 v[118:119], v[132:133], v[118:119]
	v_pk_add_f32 v[112:113], v[164:165], v[112:113]
	v_pk_add_f32 v[60:61], v[168:169], v[60:61]
	v_pk_add_f32 v[54:55], v[166:167], v[54:55]
	v_pk_add_f32 v[44:45], v[134:135], v[44:45]
	v_pk_add_f32 v[42:43], v[170:171], v[42:43]
	v_pk_add_f32 v[32:33], v[174:175], v[32:33]
	v_pk_add_f32 v[30:31], v[172:173], v[30:31]
	v_pk_add_f32 v[22:23], v[136:137], v[22:23]
	v_pk_add_f32 v[18:19], v[176:177], v[18:19]
	v_pk_add_f32 v[6:7], v[138:139], v[6:7]
	v_pk_add_f32 v[0:1], v[186:187], v[0:1]
	v_pk_add_f32 v[110:111], v[188:189], v[110:111]
	v_pk_add_f32 v[116:117], v[190:191], v[116:117]
	v_pk_add_f32 v[112:113], v[200:201], v[112:113]
	v_pk_add_f32 v[118:119], v[140:141], v[118:119]
	v_pk_add_f32 v[54:55], v[202:203], v[54:55]
	v_pk_add_f32 v[60:61], v[204:205], v[60:61]
	v_pk_add_f32 v[42:43], v[206:207], v[42:43]
	v_pk_add_f32 v[44:45], v[142:143], v[44:45]
	v_pk_add_f32 v[30:31], v[220:221], v[30:31]
	v_pk_add_f32 v[32:33], v[222:223], v[32:33]
	v_pk_add_f32 v[18:19], v[224:225], v[18:19]
	v_pk_add_f32 v[22:23], v[144:145], v[22:23]
	v_pk_add_f32 v[0:1], v[230:231], v[0:1]
	v_pk_add_f32 v[6:7], v[146:147], v[6:7]
	v_pk_add_f32 v[116:117], v[234:235], v[116:117]
	v_pk_add_f32 v[110:111], v[232:233], v[110:111]
	v_pk_add_f32 v[118:119], v[148:149], v[118:119]
	v_pk_add_f32 v[112:113], v[236:237], v[112:113]
	v_pk_add_f32 v[60:61], v[240:241], v[60:61]
	v_pk_add_f32 v[54:55], v[238:239], v[54:55]
	v_pk_add_f32 v[44:45], v[92:93], v[44:45]
	v_pk_add_f32 v[42:43], v[90:91], v[42:43]
	v_pk_add_f32 v[32:33], v[68:69], v[32:33]
	v_pk_add_f32 v[30:31], v[62:63], v[30:31]
	v_pk_add_f32 v[22:23], v[48:49], v[22:23]
	v_pk_add_f32 v[18:19], v[46:47], v[18:19]
	v_pk_add_f32 v[34:35], v[8:9], v[6:7]
	v_pk_add_f32 v[36:37], v[2:3], v[0:1]
	s_waitcnt lgkmcnt(0)
	v_lshl_add_u64 v[38:39], s[6:7], 0, v[4:5]
	v_add_u32_e32 v6, 16, v4
	v_add_u32_e32 v8, 32, v4
	v_add_u32_e32 v12, 0x1000, v4
	v_add_u32_e32 v16, 0x1020, v4
	v_lshl_add_u64 v[122:123], v[38:39], 0, s[18:19]
	global_load_dwordx4 v[0:3], v4, s[0:1]
	v_pk_mul_f32 v[26:27], v[110:111], s[24:25] op_sel_hi:[1,0]
	v_pk_mul_f32 v[96:97], v[118:119], s[24:25] op_sel_hi:[1,0]
	v_pk_mul_f32 v[98:99], v[54:55], s[24:25] op_sel_hi:[1,0]
	v_pk_mul_f32 v[100:101], v[60:61], s[24:25] op_sel_hi:[1,0]
	v_add_u32_e32 v10, 48, v4
	v_pk_mul_f32 v[102:103], v[42:43], s[24:25] op_sel_hi:[1,0]
	v_pk_mul_f32 v[104:105], v[44:45], s[24:25] op_sel_hi:[1,0]
	v_pk_mul_f32 v[106:107], v[30:31], s[24:25] op_sel_hi:[1,0]
	v_pk_mul_f32 v[108:109], v[32:33], s[24:25] op_sel_hi:[1,0]
	v_add_u32_e32 v14, 0x1010, v4
	v_pk_mul_f32 v[110:111], v[18:19], s[24:25] op_sel_hi:[1,0]
	v_add_u32_e32 v18, 0x1030, v4
	v_pk_mul_f32 v[118:119], v[36:37], s[24:25] op_sel_hi:[1,0]
	v_pk_mul_f32 v[120:121], v[34:35], s[24:25] op_sel_hi:[1,0]
	global_load_dwordx4 v[30:33], v6, s[0:1]
	global_load_dwordx4 v[34:37], v8, s[0:1]
	global_load_dwordx4 v[38:41], v10, s[0:1]
	global_load_dwordx4 v[42:45], v12, s[0:1]
	global_load_dwordx4 v[46:49], v14, s[0:1]
	global_load_dwordx4 v[50:53], v16, s[0:1]
	global_load_dwordx4 v[54:57], v18, s[0:1]
	global_load_dwordx4 v[58:61], v[122:123], off
	v_mov_b32_e32 v7, v5
	v_pk_mul_f32 v[28:29], v[116:117], s[24:25] op_sel_hi:[1,0]
	v_mov_b32_e32 v9, v5
	v_mov_b32_e32 v11, v5
	v_mov_b32_e32 v13, v5
	v_mov_b32_e32 v15, v5
	v_mov_b32_e32 v17, v5
	v_pk_mul_f32 v[116:117], v[20:21], s[24:25] op_sel_hi:[1,0]
	v_mov_b32_e32 v19, v5
	v_lshl_add_u64 v[20:21], s[6:7], 0, v[6:7]
	v_pk_mul_f32 v[94:95], v[112:113], s[24:25] op_sel_hi:[1,0]
	v_pk_mul_f32 v[112:113], v[22:23], s[24:25] op_sel_hi:[1,0]
	v_pk_mul_f32 v[114:115], v[24:25], s[24:25] op_sel_hi:[1,0]
	v_lshl_add_u64 v[22:23], s[6:7], 0, v[8:9]
	v_lshl_add_u64 v[24:25], s[6:7], 0, v[10:11]
	v_lshl_add_u64 v[62:63], s[6:7], 0, v[12:13]
	v_lshl_add_u64 v[64:65], s[6:7], 0, v[14:15]
	v_lshl_add_u64 v[66:67], s[6:7], 0, v[16:17]
	v_lshl_add_u64 v[68:69], s[6:7], 0, v[18:19]
	v_lshl_add_u64 v[124:125], v[20:21], 0, s[18:19]
	v_lshl_add_u64 v[132:133], v[22:23], 0, s[18:19]
	v_lshl_add_u64 v[134:135], v[24:25], 0, s[18:19]
	v_lshl_add_u64 v[136:137], v[62:63], 0, s[18:19]
	v_lshl_add_u64 v[24:25], v[64:65], 0, s[18:19]
	v_lshl_add_u64 v[22:23], v[66:67], 0, s[18:19]
	v_lshl_add_u64 v[20:21], v[68:69], 0, s[18:19]
	global_load_dwordx4 v[62:65], v[124:125], off
	global_load_dwordx4 v[66:69], v[132:133], off
	global_load_dwordx4 v[70:73], v[134:135], off
	global_load_dwordx4 v[74:77], v[136:137], off
	global_load_dwordx4 v[78:81], v[24:25], off
	global_load_dwordx4 v[82:85], v[22:23], off
	global_load_dwordx4 v[86:89], v[20:21], off
	global_load_dwordx4 v[90:93], v4, s[4:5]
	s_add_i32 s42, s42, s56
	s_add_u32 s10, s10, s12
	s_addc_u32 s11, s11, s13
	s_add_u32 s14, s14, s16
	s_addc_u32 s15, s15, s17
	s_add_u32 s18, s18, s20
	s_addc_u32 s19, s19, s21
	s_cmpk_lt_i32 s42, 0x2000
	s_waitcnt vmcnt(8)
	v_pk_fma_f32 v[2:3], v[2:3], v[28:29], v[60:61]
	v_pk_fma_f32 v[0:1], v[0:1], v[26:27], v[58:59]
	v_mul_f32_e32 v7, v3, v3
	v_mul_f32_e32 v4, v1, v1
	v_fmac_f32_e32 v4, v0, v0
	v_fmac_f32_e32 v7, v2, v2
	v_add_f32_e32 v4, v4, v7
	s_waitcnt vmcnt(7)
	v_pk_fma_f32 v[26:27], v[32:33], v[96:97], v[64:65]
	v_pk_fma_f32 v[28:29], v[30:31], v[94:95], v[62:63]
	s_waitcnt vmcnt(6)
	v_pk_fma_f32 v[30:31], v[36:37], v[100:101], v[68:69]
	v_pk_fma_f32 v[32:33], v[34:35], v[98:99], v[66:67]
	v_mul_f32_e32 v9, v29, v29
	v_mul_f32_e32 v11, v27, v27
	s_waitcnt vmcnt(5)
	v_pk_fma_f32 v[34:35], v[40:41], v[104:105], v[72:73]
	v_pk_fma_f32 v[36:37], v[38:39], v[102:103], v[70:71]
	v_mul_f32_e32 v13, v33, v33
	v_mul_f32_e32 v15, v31, v31
	v_fmac_f32_e32 v9, v28, v28
	v_fmac_f32_e32 v11, v26, v26
	s_waitcnt vmcnt(4)
	v_pk_fma_f32 v[38:39], v[44:45], v[108:109], v[76:77]
	v_pk_fma_f32 v[40:41], v[42:43], v[106:107], v[74:75]
	v_mul_f32_e32 v17, v37, v37
	v_mul_f32_e32 v19, v35, v35
	v_fmac_f32_e32 v13, v32, v32
	v_fmac_f32_e32 v15, v30, v30
	v_add_f32_e32 v7, v9, v11
	s_waitcnt vmcnt(3)
	v_pk_fma_f32 v[42:43], v[48:49], v[112:113], v[80:81]
	v_pk_fma_f32 v[44:45], v[46:47], v[110:111], v[78:79]
	s_waitcnt vmcnt(2)
	v_pk_fma_f32 v[46:47], v[52:53], v[116:117], v[84:85]
	s_waitcnt vmcnt(1)
	global_load_dwordx4 v[138:141], v6, s[4:5]
	global_load_dwordx4 v[142:145], v8, s[4:5]
	global_load_dwordx4 v[146:149], v10, s[4:5]
	global_load_dwordx4 v[150:153], v12, s[4:5]
	global_load_dwordx4 v[244:247], v14, s[4:5]
	global_load_dwordx4 v[248:251], v16, s[4:5]
	global_load_dwordx4 v[252:255], v18, s[4:5]
	v_pk_fma_f32 v[52:53], v[54:55], v[118:119], v[86:87]
	v_mul_f32_e32 v54, v41, v41
	v_mul_f32_e32 v55, v39, v39
	v_fmac_f32_e32 v17, v36, v36
	v_fmac_f32_e32 v19, v34, v34
	v_add_f32_e32 v9, v13, v15
	v_add_f32_e32 v4, v4, v7
	v_pk_fma_f32 v[48:49], v[50:51], v[114:115], v[82:83]
	v_pk_fma_f32 v[50:51], v[56:57], v[120:121], v[88:89]
	v_mul_f32_e32 v56, v45, v45
	v_mul_f32_e32 v57, v43, v43
	v_fmac_f32_e32 v54, v40, v40
	v_fmac_f32_e32 v55, v38, v38
	v_add_f32_e32 v11, v17, v19
	v_add_f32_e32 v4, v4, v9
	v_mul_f32_e32 v58, v49, v49
	v_mul_f32_e32 v59, v47, v47
	v_fmac_f32_e32 v56, v44, v44
	v_fmac_f32_e32 v57, v42, v42
	v_add_f32_e32 v13, v54, v55
	v_add_f32_e32 v4, v4, v11
	v_mul_f32_e32 v60, v53, v53
	v_mul_f32_e32 v61, v51, v51
	v_fmac_f32_e32 v58, v48, v48
	v_fmac_f32_e32 v59, v46, v46
	v_add_f32_e32 v15, v56, v57
	v_add_f32_e32 v4, v4, v13
	v_fmac_f32_e32 v60, v52, v52
	v_fmac_f32_e32 v61, v50, v50
	v_add_f32_e32 v17, v58, v59
	v_add_f32_e32 v4, v4, v15
	v_add_f32_e32 v19, v60, v61
	v_add_f32_e32 v4, v4, v17
	v_add_f32_e32 v4, v4, v19
	ds_swizzle_b32 v7, v4 offset:swizzle(SWAP,1)
	s_waitcnt lgkmcnt(0)
	v_add_f32_e32 v4, v4, v7
	ds_swizzle_b32 v7, v4 offset:swizzle(SWAP,2)
	s_waitcnt lgkmcnt(0)
	v_add_f32_e32 v4, v4, v7
	ds_swizzle_b32 v7, v4 offset:swizzle(SWAP,4)
	s_waitcnt lgkmcnt(0)
	v_add_f32_e32 v4, v4, v7
	ds_swizzle_b32 v7, v4 offset:swizzle(SWAP,8)
	s_waitcnt lgkmcnt(0)
	v_add_f32_e32 v4, v4, v7
	ds_swizzle_b32 v7, v4 offset:swizzle(SWAP,16)
	s_waitcnt lgkmcnt(0)
	v_add_f32_e32 v4, v4, v7
	v_mov_b32_e32 v7, v4
	s_nop 1
	v_permlane32_swap_b32_e32 v4, v7
	v_add_f32_e32 v4, v4, v7
	v_fmamk_f32 v4, v4, 0x3a000000, v129
	v_mul_f32_e32 v7, 0x4f800000, v4
	v_cmp_gt_f32_e32 vcc, s28, v4
	s_nop 1
	v_cndmask_b32_e32 v4, v4, v7, vcc
	v_sqrt_f32_e32 v7, v4
	s_nop 0
	v_add_u32_e32 v9, -1, v7
	v_add_u32_e32 v11, 1, v7
	v_fma_f32 v13, -v9, v7, v4
	v_fma_f32 v15, -v11, v7, v4
	v_cmp_ge_f32_e64 s[0:1], 0, v13
	s_nop 1
	v_cndmask_b32_e64 v7, v7, v9, s[0:1]
	v_cmp_lt_f32_e64 s[0:1], 0, v15
	s_nop 1
	v_cndmask_b32_e64 v7, v7, v11, s[0:1]
	v_mul_f32_e32 v9, 0x37800000, v7
	v_cndmask_b32_e32 v7, v7, v9, vcc
	v_cmp_class_f32_e32 vcc, v4, v130
	s_nop 1
	v_cndmask_b32_e32 v4, v7, v4, vcc
	v_div_scale_f32 v7, s[0:1], v4, v4, 1.0
	v_rcp_f32_e32 v11, v7
	v_div_scale_f32 v9, vcc, 1.0, v4, 1.0
	v_fma_f32 v13, -v7, v11, 1.0
	v_fmac_f32_e32 v11, v13, v11
	v_mul_f32_e32 v13, v9, v11
	v_fma_f32 v15, -v7, v13, v9
	v_fmac_f32_e32 v13, v15, v11
	v_fma_f32 v7, -v7, v13, v9
	v_div_fmas_f32 v7, v7, v11, v13
	v_div_fixup_f32 v4, v7, v4, 1.0
	v_pk_mul_f32 v[0:1], v[4:5], v[0:1] op_sel_hi:[0,1]
	v_pk_mul_f32 v[2:3], v[4:5], v[2:3] op_sel_hi:[0,1]
	s_waitcnt vmcnt(0)
	v_pk_mul_f32 v[2:3], v[2:3], v[92:93]
	v_pk_mul_f32 v[0:1], v[0:1], v[90:91]
	global_store_dwordx4 v[122:123], v[0:3], off
	v_pk_mul_f32 v[6:7], v[4:5], v[26:27] op_sel_hi:[0,1]
	v_pk_mul_f32 v[26:27], v[4:5], v[28:29] op_sel_hi:[0,1]
	v_pk_mul_f32 v[0:1], v[26:27], v[138:139]
	v_pk_mul_f32 v[2:3], v[6:7], v[140:141]
	global_store_dwordx4 v[124:125], v[0:3], off
	v_pk_mul_f32 v[6:7], v[4:5], v[30:31] op_sel_hi:[0,1]
	v_pk_mul_f32 v[8:9], v[4:5], v[32:33] op_sel_hi:[0,1]
	v_pk_mul_f32 v[0:1], v[8:9], v[142:143]
	v_pk_mul_f32 v[2:3], v[6:7], v[144:145]
	global_store_dwordx4 v[132:133], v[0:3], off
	v_pk_mul_f32 v[6:7], v[4:5], v[34:35] op_sel_hi:[0,1]
	v_pk_mul_f32 v[8:9], v[4:5], v[36:37] op_sel_hi:[0,1]
	v_pk_mul_f32 v[0:1], v[8:9], v[146:147]
	v_pk_mul_f32 v[2:3], v[6:7], v[148:149]
	global_store_dwordx4 v[134:135], v[0:3], off
	v_pk_mul_f32 v[6:7], v[4:5], v[38:39] op_sel_hi:[0,1]
	v_pk_mul_f32 v[8:9], v[4:5], v[40:41] op_sel_hi:[0,1]
	v_pk_mul_f32 v[0:1], v[8:9], v[150:151]
	v_pk_mul_f32 v[2:3], v[6:7], v[152:153]
	global_store_dwordx4 v[136:137], v[0:3], off
	v_pk_mul_f32 v[6:7], v[4:5], v[42:43] op_sel_hi:[0,1]
	v_pk_mul_f32 v[8:9], v[4:5], v[44:45] op_sel_hi:[0,1]
	v_pk_mul_f32 v[0:1], v[8:9], v[244:245]
	v_pk_mul_f32 v[2:3], v[6:7], v[246:247]
	global_store_dwordx4 v[24:25], v[0:3], off
	v_pk_mul_f32 v[6:7], v[4:5], v[46:47] op_sel_hi:[0,1]
	v_pk_mul_f32 v[8:9], v[4:5], v[48:49] op_sel_hi:[0,1]
	v_pk_mul_f32 v[0:1], v[8:9], v[248:249]
	v_pk_mul_f32 v[2:3], v[6:7], v[250:251]
	global_store_dwordx4 v[22:23], v[0:3], off
	v_pk_mul_f32 v[6:7], v[4:5], v[50:51] op_sel_hi:[0,1]
	v_pk_mul_f32 v[8:9], v[4:5], v[52:53] op_sel_hi:[0,1]
	v_pk_mul_f32 v[0:1], v[8:9], v[252:253]
	v_pk_mul_f32 v[2:3], v[6:7], v[254:255]
	global_store_dwordx4 v[20:21], v[0:3], off
	s_cbranch_scc1 .LBB0_1206
